# MoBA unit set-up de-serialised: block-mean loads, query loads, Q fragments and first tiles in one memory round trip
# speedup vs baseline: 1.0031x; 1.0031x over previous
; #define ATT_DMA(t, slot) do { glds16(ksrc + (long)(t) * tstep, (unsigned)__builtin_amdgcn_readfirstlane(kdst + (slot))); glds16(vsrc + (long)(t) * tstep, (unsigned)__builtin_amdgcn_readfirstlane(vdst + (slot))); } while (0)
; __device__ __forceinline__ void unpack8(const v4u w, float* f) { f[0] = bflo(w.x); f[1] = bfhi(w.x); f[2] = bflo(w.y); f[3] = bfhi(w.y); f[4] = bflo(w.z); f[5] = bfhi(w.z); f[6] = bflo(w.w); f[7] = bfhi(w.w); }
; template <class BIAS>
; __device__ __forceinline__ void attn_tiles(char* shm, const UnitIO& io, int t_begin, int t_end, const BIAS& B, int tid) {
;     ...
;     { const bf16* qp = io.Q + (long)r32 * io.qstride + hi * 8;
; #pragma unroll
;       for (int d0 = 0; d0 < 4; ++d0) qr[d0] = *reinterpret_cast<const bf16x8*>(qp + d0 * 16); }
;     ATT_DMA(t_begin, 0);
;     asm volatile("" :: "v"(qr[0]), "v"(qr[1]), "v"(qr[2]), "v"(qr[3]));
;     const int nt_ = t_end - t_begin; if (nt_ > 1) ATT_DMA(t_begin + 1, SLOTB); if (nt_ > 2) ATT_DMA(t_begin + 2, 2 * SLOTB);
; __device__ __forceinline__ void moba_unit(Frame& F, const AttnBufs& A, int b, int h, int qb) {
;     ...
;     for (int i = tid; i < 1024; i += 512) { const int j = i >> 6, d = i & 63; float v = 0.f;
;         if (j < qb) { const float* p = A.KMP + ((size_t)((b * 16 + j) * 4 + h) * 2) * 64 + d; v = p[0] + p[64]; } KM[i] = v; }
;     const size_t row0 = (size_t)b * SEQ + qb * 256 + w * 32;
;     const size_t bo = (size_t)b * BADJ;
;     const bf16* Qw = A.Q + bo + row0 * DM + h * 64;
;     float qf[32];
;     { const bf16* qp = Qw + (size_t)r32 * DM + hi * 8;
; #pragma unroll
;       for (int d0 = 0; d0 < 4; ++d0) { const v4u wv = *(const v4u*)(qp + d0 * 16); unpack8(wv, qf + 8 * d0); } }
;     __syncthreads();
.LBB0_278:
	s_and_b64 s[8:9], s[4:5], exec
	v_readlane_b32 s8, v254, 31
	v_readlane_b32 s9, v254, 33
	s_cselect_b32 s20, s8, s9
	s_and_saveexec_b64 s[8:9], s[0:1]
	s_cbranch_execz .LBB0_283
	v_ashrrev_i32_e32 v82, 6, v232
	v_lshl_add_u32 v84, v82, 2, s21
	v_add_u32_e32 v86, 32, v84
	v_ashrrev_i32_e32 v85, 31, v84
	v_ashrrev_i32_e32 v87, 31, v86
	v_lshlrev_b64 v[84:85], 9, v[84:85]
	v_lshlrev_b64 v[86:87], 9, v[86:87]
	v_lshl_add_u64 v[84:85], v[158:159], 0, v[84:85]
	v_lshl_add_u64 v[86:87], v[158:159], 0, v[86:87]
	global_load_dword v90, v[84:85], off
	global_load_dword v91, v[84:85], off offset:256
	global_load_dword v92, v[86:87], off
	global_load_dword v93, v[86:87], off offset:256
.LBB0_283:
	s_or_b64 exec, exec, s[8:9]
	s_xor_b64 s[8:9], s[4:5], -1
	s_lshl_b32 s22, s20, 8
	v_readlane_b32 s4, v254, 36
	s_add_u32 s10, s4, s22
	v_readlane_b32 s4, v254, 40
	s_addc_u32 s11, s4, 0
	s_lshl_b64 s[4:5], s[10:11], 11
	v_readlane_b32 s12, v254, 43
	s_add_u32 s4, s12, s4
	v_readlane_b32 s12, v254, 46
	s_addc_u32 s5, s12, s5
	v_mov_b32_e32 v169, v1
	v_lshl_add_u64 v[2:3], s[4:5], 0, v[168:169]
	v_mov_b32_e32 v171, v1
	v_lshl_add_u64 v[2:3], v[2:3], 0, v[170:171]
	flat_load_dwordx4 v[14:17], v[2:3]
	flat_load_dwordx4 v[10:13], v[2:3] offset:32
	flat_load_dwordx4 v[6:9], v[2:3] offset:64
	s_nop 0
	flat_load_dwordx4 v[2:5], v[2:3] offset:96
	v_lshlrev_b32_e32 v148, 1, v154
	v_mov_b32_e32 v149, v1
	v_lshl_add_u64 v[212:213], s[4:5], 0, v[132:133]
	v_lshl_add_u64 v[212:213], v[212:213], 0, v[148:149]
	flat_load_dwordx4 v[66:69], v[212:213]
	flat_load_dwordx4 v[70:73], v[212:213] offset:32
	flat_load_dwordx4 v[74:77], v[212:213] offset:64
	flat_load_dwordx4 v[78:81], v[212:213] offset:96
	v_readfirstlane_b32 s27, v232
	s_ashr_i32 s16, s27, 6
	s_lshl_b32 s12, s16, 4
	v_and_or_b32 v222, s12, 48, v178
	s_ashr_i32 s12, s27, 3
	s_lshl_b32 s14, s16, 3
	s_andn2_b32 s12, s12, 31
	s_ashr_i32 s15, s14, 31
	s_ashr_i32 s13, s12, 31
	v_lshlrev_b32_e32 v222, 11, v222
	v_mov_b32_e32 v223, v1
	s_lshl_b64 s[100:101], s[14:15], 1
	v_lshl_add_u64 v[222:223], s[30:31], 0, v[222:223]
	s_lshl_b64 s[12:13], s[12:13], 1
	s_lshl_b32 s29, s16, 10
	v_lshl_add_u64 v[212:213], v[156:157], 0, s[100:101]
	v_lshl_add_u64 v[212:213], v[212:213], 0, v[244:245]
	v_lshl_add_u64 v[222:223], v[222:223], 0, s[12:13]
	v_lshlrev_b32_e32 v150, 1, v144
	v_mov_b32_e32 v151, v1
	v_lshl_add_u64 v[222:223], v[222:223], 0, v[150:151]
	s_add_i32 s33, s29, 0x8000
	s_mov_b64 s[100:101], 0x20000
	s_mov_b32 m0, s29
	s_add_i32 s12, s29, 0x2000
	global_load_lds_dwordx4 v[212:213], off
	s_mov_b32 m0, s33
	s_add_i32 s13, s33, 0x2000
	global_load_lds_dwordx4 v[222:223], off
	v_lshl_add_u64 v[212:213], v[212:213], 0, s[100:101]
	v_lshl_add_u64 v[222:223], v[222:223], 0, s[100:101]
	s_mov_b32 m0, s12
	s_add_i32 s12, s29, 0x4000
	global_load_lds_dwordx4 v[212:213], off
	s_mov_b32 m0, s13
	s_add_i32 s13, s33, 0x4000
	global_load_lds_dwordx4 v[222:223], off
	v_lshl_add_u64 v[212:213], v[212:213], 0, s[100:101]
	v_lshl_add_u64 v[222:223], v[222:223], 0, s[100:101]
	s_mov_b32 m0, s12
	s_nop 0
	global_load_lds_dwordx4 v[212:213], off
	s_mov_b32 m0, s13
	s_nop 0
	global_load_lds_dwordx4 v[222:223], off
	s_and_saveexec_b64 s[12:13], s[0:1]
	s_waitcnt vmcnt(14)
	v_add_f32_e32 v90, v90, v91
	v_add_f32_e32 v92, v92, v93
	v_cmp_gt_i32_e32 vcc, s20, v82
	v_add_u32_e32 v83, 8, v82
	s_nop 0
	v_cndmask_b32_e32 v90, 0, v90, vcc
	v_cmp_gt_i32_e32 vcc, s20, v83
	s_nop 1
	v_cndmask_b32_e32 v92, 0, v92, vcc
	ds_write_b32 v161, v90
	ds_write_b32 v161, v92 offset:2048
	s_or_b64 exec, exec, s[12:13]
	s_cmp_eq_u32 s20, 0
	s_waitcnt vmcnt(0) lgkmcnt(0)
	s_barrier
	s_cbranch_scc1 .LBB0_293
	v_lshlrev_b32_e32 v18, 16, v14
	v_and_b32_e32 v14, 0xffff0000, v14
	v_lshlrev_b32_e32 v19, 16, v15
	v_and_b32_e32 v15, 0xffff0000, v15
	v_lshlrev_b32_e32 v20, 16, v16
	v_and_b32_e32 v16, 0xffff0000, v16
	v_lshlrev_b32_e32 v21, 16, v17
	v_and_b32_e32 v17, 0xffff0000, v17
	v_lshlrev_b32_e32 v22, 16, v10
	v_and_b32_e32 v23, 0xffff0000, v10
	v_lshlrev_b32_e32 v24, 16, v11
	v_and_b32_e32 v25, 0xffff0000, v11
	v_lshlrev_b32_e32 v26, 16, v12
	v_and_b32_e32 v12, 0xffff0000, v12
	v_lshlrev_b32_e32 v27, 16, v13
	v_and_b32_e32 v13, 0xffff0000, v13
	v_lshlrev_b32_e32 v28, 16, v6
	v_and_b32_e32 v29, 0xffff0000, v6
	v_lshlrev_b32_e32 v30, 16, v7
	v_and_b32_e32 v31, 0xffff0000, v7
	v_lshlrev_b32_e32 v32, 16, v8
	v_and_b32_e32 v33, 0xffff0000, v8
	v_lshlrev_b32_e32 v34, 16, v9
	v_and_b32_e32 v35, 0xffff0000, v9
	v_lshlrev_b32_e32 v7, 16, v2
	v_lshlrev_b32_e32 v6, 16, v4
	v_and_b32_e32 v9, 0xffff0000, v2
	v_and_b32_e32 v8, 0xffff0000, v4
	v_lshlrev_b32_e32 v11, 16, v3
	v_lshlrev_b32_e32 v10, 16, v5
	v_and_b32_e32 v3, 0xffff0000, v3
	v_and_b32_e32 v2, 0xffff0000, v5
	v_mov_b32_e32 v39, 0xff800000
	v_mov_b32_e32 v38, -1
	s_mov_b32 s23, 0
	s_mov_b32 s26, 0
	v_mov_b32_e32 v4, -1
	v_mov_b32_e32 v5, -1
	v_mov_b32_e32 v36, 0xff800000
	v_mov_b32_e32 v37, 0xff800000
